# half of the workgroups run the PEER table conversion (phase 7) before the output projection (phase 6): independent phases, HBM-bound vs MFMA-bound overlap
# speedup vs baseline: 1.0079x; 1.0079x over previous
_Z4mega4Args:
	s_mov_b32 s95, 0
	s_load_dwordx2 s[40:41], s[0:1], 0xc0
	v_readfirstlane_b32 s25, v0
	s_andn2_b32 s25, s25, 63
	v_mbcnt_lo_u32_b32 v0, -1, 0
	v_mbcnt_hi_u32_b32 v0, -1, v0
	s_mov_b32 s24, s2
	v_or_b32_e32 v0, s25, v0
	v_cmp_gt_i32_e32 vcc, 2, v0
	s_and_saveexec_b64 s[2:3], vcc
	s_cbranch_execz .LBB0_2
	s_mov_b64 s[4:5], src_shared_base
	s_add_i32 s4, 0, 0x23fc0
	v_lshl_add_u32 v2, v0, 2, s4
	v_mov_b32_e32 v3, s5
	v_mov_b32_e32 v1, 0
	flat_store_dword v[2:3], v1 sc0 sc1
	s_waitcnt vmcnt(0)

.Lp6_entry:
	s_lshr_b32 s94, s24, 3
	s_and_b32 s94, s94, 1
	s_cmp_eq_u32 s94, 0
	s_cbranch_scc1 .Lp6_body
	s_cmp_eq_u32 s95, 1
	s_cbranch_scc1 .Lp6_body
	s_branch .Lp7_body
.Lp6_body:
	s_cmpk_lt_i32 s24, 0x200
	s_cselect_b64 s[4:5], -1, 0
	s_ashr_i32 s29, s24, 31
	v_mbcnt_lo_u32_b32 v8, -1, 0
	v_mbcnt_hi_u32_b32 v8, -1, v8
	s_cmpk_gt_i32 s24, 0x1ff
	v_or_b32_e32 v0, s25, v8
	s_mov_b64 s[2:3], s[0:1]
	v_readfirstlane_b32 s20, v0
	s_cbranch_scc1 .LBB0_833
	s_ashr_i32 s6, s24, 31
	s_lshr_b32 s6, s6, 29
	s_add_i32 s6, s24, s6
	s_ashr_i32 s7, s6, 3
	s_and_b32 s6, s6, -8
	s_sub_i32 s6, s24, s6
	s_lshl_b32 s9, s6, 6
	s_mul_i32 s8, s6, 0x41
	s_cmp_lt_i32 s6, 0
	s_cselect_b32 s6, s8, s9
	s_add_i32 s6, s6, s7
	s_ashr_i32 s7, s6, 31
	s_lshr_b32 s7, s7, 26
	s_add_i32 s7, s6, s7
	s_ashr_i32 s8, s7, 6
	s_and_b32 s7, s7, 0xffc0
	s_sub_i32 s6, s6, s7
	s_bfe_i32 s7, s6, 0x80000
	s_bfe_u32 s7, s7, 0x3000c
	s_add_i32 s7, s6, s7
	s_bfe_i32 s9, s7, 0x80000
	s_and_b32 s7, s7, 0xf8
	s_sub_i32 s6, s6, s7
	s_lshl_b32 s8, s8, 3
	s_sext_i32_i16 s9, s9
	s_sext_i32_i8 s6, s6
	s_add_i32 s42, s8, s6
	s_ashr_i32 s44, s9, 3

.LBB0_869:
	s_cmp_lt_i32 s40, 8
	s_cselect_b64 s[2:3], -1, 0
	s_cmp_gt_i32 s41, 7
	s_cselect_b64 s[4:5], -1, 0
	s_and_b64 s[10:11], s[2:3], s[4:5]
	s_andn2_b64 vcc, exec, s[10:11]
	s_cbranch_vccnz .LBB0_911
	s_cmp_eq_u32 s95, 1
	s_cbranch_scc1 .LBB0_911
.Lp7_body:
	s_mov_b64 s[6:7], s[0:1]
	v_mbcnt_lo_u32_b32 v130, -1, 0
	v_mbcnt_hi_u32_b32 v130, -1, v130
	s_load_dwordx4 s[12:15], s[6:7], 0x98
	s_load_dwordx2 s[4:5], s[6:7], 0xb8
	s_load_dword s17, s[0:1], 0xc8
	v_or_b32_e32 v2, s25, v130
	s_movk_i32 s2, 0x800
	v_readfirstlane_b32 s16, v2
	v_cmp_gt_i32_e32 vcc, s2, v2
	s_waitcnt vmcnt(0) lgkmcnt(0)
	s_barrier
	s_and_saveexec_b64 s[2:3], vcc
	s_cbranch_execz .LBB0_873
	s_load_dwordx2 s[8:9], s[6:7], 0x20
	v_lshlrev_b32_e32 v3, 2, v2
	s_mov_b64 s[6:7], 0
	v_mov_b32_e32 v1, 0
	s_movk_i32 s18, 0x5ff
	s_waitcnt lgkmcnt(0)
	s_add_u32 s8, s8, 0x6000
	s_addc_u32 s9, s9, 0

.Lp7_exit:
	s_cmp_eq_u32 s94, 1
	s_cbranch_scc0 .LBB0_911
	s_cmp_eq_u32 s95, 0
	s_cbranch_scc0 .LBB0_911
	s_mov_b32 s95, 1
	s_waitcnt vmcnt(0) lgkmcnt(0)
	s_barrier
	s_branch .Lp6_entry

	.amdhsa_kernel _Z4mega4Args
		.amdhsa_group_segment_fixed_size 0
		.amdhsa_private_segment_fixed_size 0
		.amdhsa_kernarg_size 456
		.amdhsa_user_sgpr_count 2
		.amdhsa_user_sgpr_dispatch_ptr 0
		.amdhsa_user_sgpr_queue_ptr 0
		.amdhsa_user_sgpr_kernarg_segment_ptr 1
		.amdhsa_user_sgpr_dispatch_id 0
		.amdhsa_user_sgpr_kernarg_preload_length 0
		.amdhsa_user_sgpr_kernarg_preload_offset 0
		.amdhsa_user_sgpr_private_segment_size 0
		.amdhsa_uses_dynamic_stack 0
		.amdhsa_enable_private_segment 0
		.amdhsa_system_sgpr_workgroup_id_x 1
		.amdhsa_system_sgpr_workgroup_id_y 0
		.amdhsa_system_sgpr_workgroup_id_z 0
		.amdhsa_system_sgpr_workgroup_info 0
		.amdhsa_system_vgpr_workitem_id 0
		.amdhsa_next_free_vgpr 256
		.amdhsa_next_free_sgpr 96
		.amdhsa_accum_offset 256
		.amdhsa_reserve_vcc 1
		.amdhsa_float_round_mode_32 0
		.amdhsa_float_round_mode_16_64 0
		.amdhsa_float_denorm_mode_32 3
		.amdhsa_float_denorm_mode_16_64 3
		.amdhsa_dx10_clamp 1
		.amdhsa_ieee_mode 1
		.amdhsa_fp16_overflow 0
		.amdhsa_tg_split 0
		.amdhsa_exception_fp_ieee_invalid_op 0
		.amdhsa_exception_fp_denorm_src 0
		.amdhsa_exception_fp_ieee_div_zero 0
		.amdhsa_exception_fp_ieee_overflow 0
		.amdhsa_exception_fp_ieee_underflow 0
		.amdhsa_exception_fp_ieee_inexact 0
		.amdhsa_exception_int_div_zero 0
	.end_amdhsa_kernel

amdhsa.kernels:
  - .agpr_count:     0
    .args:
      - .offset:         0
        .size:           200
        .value_kind:     by_value
      - .offset:         200
        .size:           4
        .value_kind:     hidden_block_count_x
      - .offset:         204
        .size:           4
        .value_kind:     hidden_block_count_y
      - .offset:         208
        .size:           4
        .value_kind:     hidden_block_count_z
      - .offset:         212
        .size:           2
        .value_kind:     hidden_group_size_x
      - .offset:         214
        .size:           2
        .value_kind:     hidden_group_size_y
      - .offset:         216
        .size:           2
        .value_kind:     hidden_group_size_z
      - .offset:         218
        .size:           2
        .value_kind:     hidden_remainder_x
      - .offset:         220
        .size:           2
        .value_kind:     hidden_remainder_y
      - .offset:         222
        .size:           2
        .value_kind:     hidden_remainder_z
      - .offset:         240
        .size:           8
        .value_kind:     hidden_global_offset_x
      - .offset:         248
        .size:           8
        .value_kind:     hidden_global_offset_y
      - .offset:         256
        .size:           8
        .value_kind:     hidden_global_offset_z
      - .offset:         264
        .size:           2
        .value_kind:     hidden_grid_dims
      - .offset:         320
        .size:           4
        .value_kind:     hidden_dynamic_lds_size
    .group_segment_fixed_size: 0
    .kernarg_segment_align: 8
    .kernarg_segment_size: 456
    .language:       OpenCL C
    .language_version:
      - 2
      - 0
    .max_flat_workgroup_size: 512
    .name:           _Z4mega4Args
    .private_segment_fixed_size: 0
    .sgpr_count:     102
    .sgpr_spill_count: 0
    .symbol:         _Z4mega4Args.kd
    .uniform_work_group_size: 1
    .uses_dynamic_stack: false
    .vgpr_count:     256
    .vgpr_spill_count: 0
    .wavefront_size: 64
